# in-proj and gates GEMM unit order remapped to 8x4 row/col blocks per XCD round (L2 sharing)
# speedup vs baseline: 1.0236x; 1.0108x over previous
.LBB0_210:
	s_or_b64 exec, exec, s[0:1]
	s_waitcnt lgkmcnt(0)
	s_barrier
	s_load_dword s5, s[94:95], 0x180
	s_mov_b64 s[0:1], src_shared_base
	v_writelane_b32 v252, s0, 6
	s_mov_b32 s51, 0
	s_movk_i32 s93, 0x180
	v_writelane_b32 v252, s1, 7
	s_waitcnt lgkmcnt(0)
	s_ashr_i32 s7, s5, 3
	v_readlane_b32 s4, v252, 0
	s_ashr_i32 s6, s4, 3
	s_cmpk_lt_i32 s6, 0x120
	s_cselect_b64 s[0:1], -1, 0
	v_writelane_b32 v252, s0, 8
	s_movk_i32 s77, 0x70
	s_mov_b32 s85, 0x800000
	v_writelane_b32 v252, s1, 9
	s_lshl_b32 s0, s4, 4
	s_and_b32 s8, s0, 0x70
	s_lshr_b32 s100, s6, 5
	s_and_b32 s101, s6, 31
	s_lshr_b32 s0, s100, 2
	s_lshl_b32 s0, s0, 3
	s_and_b32 s1, s101, 7
	s_add_i32 s0, s0, s1
	s_and_b32 s10, s100, 3
	s_lshl_b32 s10, s10, 2
	s_lshr_b32 s1, s101, 3
	s_add_i32 s10, s10, s1
	s_and_b32 s1, s101, 15
	s_lshr_b32 s11, s101, 4
	s_add_i32 s11, s11, 16
	s_cmp_lt_u32 s100, 8
	s_cselect_b32 s0, s0, s1
	s_cselect_b32 s10, s10, s11
	s_add_i32 s2, s0, s8
	s_ashr_i32 s11, s10, 31
	s_lshl_b64 s[0:1], s[10:11], 19
	v_writelane_b32 v252, s0, 10
	s_waitcnt vmcnt(0)
	v_mov_b32_e32 v3, 0
	v_mov_b32_e32 v220, 0x1000
	v_writelane_b32 v252, s1, 11
	s_mov_b32 s0, s10
	v_writelane_b32 v252, s0, 12
	v_mov_b32_e32 v221, 0x2000
	v_mov_b32_e32 v219, 0x3b808081
	v_writelane_b32 v252, s1, 13
	s_add_i32 s0, s10, -12
	s_cmp_lt_u32 s0, 3
	s_cselect_b64 s[0:1], -1, 0
	v_writelane_b32 v252, s0, 14
	s_ashr_i32 s3, s2, 31
	v_mbcnt_hi_u32_b32 v214, -1, v42
	v_writelane_b32 v252, s1, 15
	s_lshl_b64 s[0:1], s[2:3], 19
	v_writelane_b32 v252, s0, 16
	v_mov_b32_e32 v226, 0x180
	v_mov_b32_e32 v232, 0x100000
	v_writelane_b32 v252, s1, 17
	s_mov_b32 s0, s2
	v_writelane_b32 v252, s0, 18
	v_mov_b32_e32 v227, 0x2080
	v_mov_b32_e32 v228, 0xff61b1e6
	v_writelane_b32 v252, s1, 19
	s_lshl_b32 s0, s2, 8
	s_cmpk_eq_i32 s5, 0x100
	v_writelane_b32 v252, s0, 20
	s_cselect_b64 s[0:1], -1, 0
	s_ashr_i32 s10, s4, 4
	v_writelane_b32 v252, s0, 21
	s_ashr_i32 s11, s10, 31
	s_and_b32 s9, s4, 15
	v_writelane_b32 v252, s1, 22
	s_lshl_b64 s[0:1], s[10:11], 2
	s_getpc_b64 s[2:3]
	s_add_u32 s2, s2, __const._Z4mega6Params.SLOT@rel32@lo+4
	s_addc_u32 s3, s3, __const._Z4mega6Params.SLOT@rel32@hi+12
	s_add_u32 s0, s2, s0
	s_addc_u32 s1, s3, s1
	v_writelane_b32 v252, s0, 23
	s_mov_b32 s2, s10
	v_mov_b32_e32 v233, 0xc8
	v_writelane_b32 v252, s1, 24
	s_lshl_b32 s0, s9, 5
	v_writelane_b32 v252, s0, 25
	s_add_i32 s0, s4, 0xffffff70
	v_writelane_b32 v252, s2, 26
	s_add_i32 s1, s10, -9
	s_cmp_lt_u32 s1, 4
	s_cselect_b32 s0, s0, 0x100000
	v_writelane_b32 v252, s3, 27
	v_writelane_b32 v252, s0, 28
	s_lshl_b32 s0, s9, 3
	s_add_i32 s1, s0, -1
	s_lshl_b32 s0, s9, 2
	v_writelane_b32 v252, s9, 29
	s_sub_i32 s0, s1, s0
	v_writelane_b32 v252, s1, 30
	s_cmpk_lt_i32 s6, 0x100
	v_writelane_b32 v252, s0, 31
	s_cselect_b64 s[0:1], -1, 0
	v_writelane_b32 v252, s0, 32
	v_mov_b32_e32 v234, 0xc0
	s_movk_i32 s91, 0xc0
	v_writelane_b32 v252, s1, 33
	s_lshr_b32 s100, s6, 5
	s_and_b32 s101, s6, 31
	s_lshr_b32 s1, s100, 2
	s_lshl_b32 s1, s1, 3
	s_and_b32 s0, s101, 7
	s_add_i32 s1, s1, s0
	s_and_b32 s2, s100, 3
	s_lshl_b32 s2, s2, 2
	s_lshr_b32 s0, s101, 3
	s_add_i32 s2, s2, s0
	v_writelane_b32 v252, s8, 34
	s_add_i32 s8, s1, s8
	s_add_i32 s3, s2, 18
	s_cmp_lt_i32 s2, 0
	s_cselect_b64 s[0:1], -1, 0
	v_writelane_b32 v252, s0, 35
	s_movk_i32 s33, 0x2400
	s_movk_i32 s96, 0xc00
	v_writelane_b32 v252, s1, 36
	s_and_b64 s[0:1], s[0:1], exec
	s_cselect_b32 s50, s3, s2
	v_writelane_b32 v252, s3, 37
	s_lshl_b64 s[0:1], s[50:51], 19
	s_add_i32 s2, s2, 6
	v_writelane_b32 v252, s0, 38
	s_cmp_lt_u32 s2, 3
	s_movk_i32 s97, 0x60
	v_writelane_b32 v252, s1, 39
	s_cselect_b64 s[0:1], -1, 0
	v_writelane_b32 v252, s0, 40
	s_ashr_i32 s9, s8, 31
	s_mov_b32 s83, 0x2aaaaaab
	v_writelane_b32 v252, s1, 41
	s_lshl_b64 s[0:1], s[8:9], 19
	v_writelane_b32 v252, s0, 42
	s_movk_i32 s86, 0xff40
	s_movk_i32 s87, 0x7fff
	v_writelane_b32 v252, s1, 43
	s_mov_b32 s0, s8
	v_writelane_b32 v252, s0, 44
	s_movk_i32 s88, 0x9ff
	s_movk_i32 s89, 0x2080
	v_writelane_b32 v252, s1, 45
	s_lshl_b32 s0, s8, 8
	s_cmpk_lt_i32 s6, 0x80
	v_writelane_b32 v252, s0, 46
	s_cselect_b64 s[0:1], -1, 0
	v_writelane_b32 v252, s0, 47
	s_mov_b32 s90, 0xff61b1e6
	s_mov_b64 s[60:61], 0x80
	v_writelane_b32 v252, s1, 48
	s_and_b32 s0, s4, 7
	s_cmp_lt_i32 s6, 64
	s_cselect_b64 s[2:3], -1, 0
	v_writelane_b32 v252, s2, 49
	s_mov_b64 s[40:41], 0x2200
	s_mov_b64 s[70:71], 0x2000
	v_writelane_b32 v252, s3, 50
	v_writelane_b32 v252, s0, 51
	s_lshl_b32 s2, s0, 4
	s_lshr_b32 s0, s6, 30
	s_add_i32 s0, s6, s0
	s_ashr_i32 s1, s0, 2
	v_writelane_b32 v252, s2, 52
	s_add_i32 s1, s2, s1
	s_and_b32 s0, s0, -4
	v_writelane_b32 v252, s1, 53
	s_sub_i32 s8, s6, s0
	s_lshl_b32 s0, s5, 3
	v_writelane_b32 v252, s0, 54
	s_mov_b64 s[80:81], 0x48000
	s_mov_b32 s82, 0x3e38aa3b
	v_writelane_b32 v252, s1, 55
	s_lshl_b32 s0, s5, 5
	v_writelane_b32 v252, s0, 56
	s_ashr_i32 s0, s4, 6
	v_writelane_b32 v252, s0, 57
	s_and_b32 s0, s6, 7
	s_cmp_lt_u32 s0, 4
	v_writelane_b32 v252, s0, 58
	s_cselect_b64 s[0:1], -1, 0
	s_abs_i32 s2, s7
	v_cvt_f32_u32_e32 v1, s2
	v_writelane_b32 v252, s0, 59
	s_mov_b32 s5, s51
	s_ashr_i32 s9, s8, 31
	v_rcp_iflag_f32_e32 v1, v1
	v_writelane_b32 v252, s1, 60
	v_writelane_b32 v252, s7, 61
	s_and_b32 s1, s6, 1
	v_mul_f32_e32 v1, 0x4f7ffffe, v1
	v_cvt_u32_f32_e32 v1, v1
	v_writelane_b32 v252, s6, 62
	s_lshl_b32 s4, s1, 7
	v_writelane_b32 v252, s4, 63
	s_lshl_b32 s1, s1, 1
	s_lshl_b32 s0, s6, 18
	v_writelane_b32 v253, s5, 0
	v_writelane_b32 v253, s1, 1
	v_writelane_b32 v253, s2, 2
	s_sub_i32 s1, 0, s2
	v_readfirstlane_b32 s2, v1
	s_mul_i32 s1, s1, s2
	s_mul_hi_u32 s1, s2, s1
	s_add_i32 s1, s2, s1
	v_writelane_b32 v253, s1, 3
	s_add_i32 s1, 0, 0x26280
	v_writelane_b32 v253, s1, 4
	s_add_i32 s1, 0, 0x26284
	v_writelane_b32 v253, s1, 5
	s_add_i32 s1, 0, 0x26288
	v_writelane_b32 v253, s1, 6
	s_add_i32 s1, 0, 0x18400
	v_writelane_b32 v253, s1, 7
	s_add_i32 s1, 0, 0x184c0
	v_writelane_b32 v253, s1, 8
	s_add_i32 s1, 0, 0x17700
	v_writelane_b32 v253, s1, 9
	s_add_i32 s1, 0, 0x17800
	v_writelane_b32 v253, s1, 10
	s_add_i32 s1, 0, 0x17100
	v_writelane_b32 v253, s1, 11
	s_add_i32 s1, 0, 0xb600
	v_writelane_b32 v253, s1, 12
	s_add_i32 s1, 0, 0x1e650
	v_writelane_b32 v253, s1, 13
	s_add_i32 s1, 0, 0x5c00
	v_writelane_b32 v253, s1, 14
	s_add_i32 s1, 0, 0x15940
	v_writelane_b32 v253, s1, 15
	s_add_i32 s1, 0, 0x15840
	v_writelane_b32 v253, s1, 16
	s_add_i32 s1, 0, 0x15f40
	v_writelane_b32 v253, s1, 17
	s_add_i32 s1, 0, 0x15240
	v_writelane_b32 v253, s1, 18
	s_add_i32 s1, 0, 0x11640
	v_writelane_b32 v253, s1, 19
	s_add_i32 s1, 0, 0x14640
	v_writelane_b32 v253, s1, 20
	s_add_i32 s1, 0, 0x14c40
	v_writelane_b32 v253, s1, 21
	s_add_i32 s1, 0, 0x15c40
	v_writelane_b32 v253, s1, 22
	s_add_i32 s1, 0, 0x15d00
	v_writelane_b32 v253, s1, 23
	s_add_i32 s1, 0, 0x15dc0
	v_writelane_b32 v253, s1, 24
	s_add_i32 s1, 0, 0x15e80
	v_writelane_b32 v253, s1, 25
	s_add_i32 s1, 0, 0x7e40
	v_writelane_b32 v253, s1, 26
	s_add_i32 s1, 0, 0x8280
	v_writelane_b32 v253, s1, 27
	s_add_i32 s1, 0, 0xa094
	v_writelane_b32 v253, s1, 28
	s_add_i32 s1, 0, 0x10380
	v_writelane_b32 v253, s1, 29
	s_add_i32 s1, 0, 0x12380
	v_writelane_b32 v253, s1, 30
	s_add_i32 s1, 0, 0x14380
	v_writelane_b32 v253, s1, 31
	s_add_i32 s1, 0, 0x16380
	v_writelane_b32 v253, s1, 32
	s_add_i32 s1, 0, 0x18380
	v_writelane_b32 v253, s1, 33
	s_add_i32 s1, 0, 0x1a380
	v_writelane_b32 v253, s1, 34
	s_add_i32 s1, 0, 0x1c380
	v_writelane_b32 v253, s1, 35
	s_add_i32 s1, 0, 0x1e380
	v_writelane_b32 v253, s1, 36
	s_add_i32 s1, 0, 0x10100
	v_writelane_b32 v253, s1, 37
	s_add_i32 s1, 0, 0x12100
	v_writelane_b32 v253, s1, 38
	s_add_i32 s1, 0, 0x16100
	v_writelane_b32 v253, s1, 39
	s_add_i32 s1, 0, 0x20060
	v_writelane_b32 v253, s1, 40
	s_add_i32 s1, 0, 0x20004
	v_writelane_b32 v253, s1, 41
	s_add_i32 s1, 0, 0x2000c
	v_writelane_b32 v253, s1, 42
	s_add_i32 s1, 0, 0x20014
	v_writelane_b32 v253, s1, 43
	s_add_i32 s1, 0, 0x2001c
	v_writelane_b32 v253, s1, 44
	s_add_i32 s1, 0, 0x20024
	v_writelane_b32 v253, s1, 45
	s_add_i32 s1, 0, 0x2002c
	v_writelane_b32 v253, s1, 46
	s_add_i32 s1, 0, 0x20034
	v_writelane_b32 v253, s1, 47
	s_add_i32 s1, 0, 0x2003c
	v_writelane_b32 v253, s1, 48
	s_add_i32 s1, 0, 0x20044
	v_writelane_b32 v253, s1, 49
	s_add_i32 s1, 0, 0x2004c
	v_writelane_b32 v253, s1, 50
	s_add_i32 s1, 0, 0x20054
	s_and_b32 s0, s0, 0xc0000
	v_writelane_b32 v253, s1, 51
	s_add_i32 s1, 0, 0x2005c
	v_writelane_b32 v253, s1, 52
	s_lshl_b32 s0, s0, 1
	v_writelane_b32 v253, s0, 53
	s_add_i32 s69, 0, 0x14100
	v_mov_b32_e32 v1, 0x358637bd
	v_writelane_b32 v253, s1, 54
	s_mov_b32 s0, 0
	v_writelane_b32 v253, s0, 55
	s_mov_b32 s0, s8
	v_writelane_b32 v253, s0, 56
	s_mov_b64 s[4:5], 0
	s_mov_b32 s84, 0x3b808081
	v_writelane_b32 v253, s1, 57
	s_lshl_b64 s[0:1], s[8:9], 19
	v_writelane_b32 v253, s0, 58
	s_nop 1
	v_writelane_b32 v253, s1, 59
	s_mov_b64 s[0:1], -1
	v_writelane_b32 v253, s0, 60
	s_nop 1
	v_writelane_b32 v253, s1, 61
	v_writelane_b32 v253, s69, 62
	v_writelane_b32 v253, s92, 63
	s_nop 1
	v_writelane_b32 v254, s93, 0
	v_writelane_b32 v254, s94, 1
	s_nop 1
	v_writelane_b32 v254, s95, 2
	s_branch .LBB0_213

.LBB0_220:
	s_add_i32 s45, s48, 1
	v_readlane_b32 s15, v252, 61
	s_mul_i32 s15, s45, s15
	v_readlane_b32 s17, v252, 62
	s_add_i32 s15, s15, s17
	s_cmpk_lt_i32 s15, 0x120
	s_cselect_b64 s[24:25], -1, 0
	s_cmpk_gt_i32 s15, 0x11f
	s_cselect_b64 s[18:19], -1, 0
	s_and_b64 vcc, exec, s[18:19]
	s_cbranch_vccnz .LBB0_222
	s_lshr_b32 s100, s15, 5
	s_and_b32 s101, s15, 31
	s_lshr_b32 s14, s100, 2
	s_lshl_b32 s14, s14, 3
	s_and_b32 vcc_lo, s101, 7
	s_add_i32 s14, s14, vcc_lo
	s_and_b32 s16, s100, 3
	s_lshl_b32 s16, s16, 2
	s_lshr_b32 vcc_lo, s101, 3
	s_add_i32 s16, s16, vcc_lo
	s_and_b32 vcc_lo, s101, 15
	s_lshr_b32 vcc_hi, s101, 4
	s_add_i32 vcc_hi, vcc_hi, 16
	s_cmp_lt_u32 s100, 8
	s_cselect_b32 s14, s14, vcc_lo
	s_cselect_b32 s16, s16, vcc_hi
	v_readlane_b32 s100, v252, 34
	s_add_i32 s14, s14, s100

.LBB0_1971:
	s_add_i32 s57, s50, 1
	v_readlane_b32 s21, v252, 61
	s_mul_i32 s21, s57, s21
	v_readlane_b32 s22, v252, 62
	s_add_i32 s21, s21, s22
	s_cmpk_lt_i32 s21, 0x100
	s_cselect_b64 s[30:31], -1, 0
	s_cmpk_gt_i32 s21, 0xff
	s_cselect_b64 s[22:23], -1, 0
	s_and_b64 vcc, exec, s[22:23]
	s_cbranch_vccnz .LBB0_1973
	s_lshr_b32 s100, s21, 5
	s_and_b32 s101, s21, 31
	s_lshr_b32 s20, s100, 2
	s_lshl_b32 s20, s20, 3
	s_and_b32 s26, s101, 7
	s_add_i32 s20, s20, s26
	s_and_b32 s26, s100, 3
	s_lshl_b32 s26, s26, 2
	s_lshr_b32 s21, s101, 3
	s_add_i32 s21, s21, s26
	v_readlane_b32 s27, v252, 34
	s_add_i32 s20, s20, s27
	s_add_i32 s56, s21, 18
